# attention: K/V LDS staging ring deepened to 4 slots (second buffer pair at +64 KB, base registers toggled per iteration) so the buffer-reuse workgroup barrier is deleted from the steady-state loop: on
# speedup vs baseline: 1.0032x; 1.0032x over previous
.LBB0_581:
	s_ashr_i32 s23, s22, 31
	s_lshl_b64 s[4:5], s[22:23], 2
	s_ashr_i32 s24, s31, 31
	s_add_u32 s1, s4, s31
	s_addc_u32 s4, s5, s24
	s_mulk_i32 s4, 0xc0
	s_mul_hi_u32 s5, s1, 0xc0
	s_add_i32 s5, s5, s4
	s_mulk_i32 s1, 0xc0
	s_add_u32 s4, s8, s1
	s_addc_u32 s5, s9, s5
	s_ashr_i32 s1, s0, 31
	s_lshl_b64 s[6:7], s[0:1], 2
	s_add_u32 s1, s6, s31
	s_addc_u32 s24, s7, s24
	s_mul_i32 s6, s24, 0x110000
	s_mul_hi_u32 s7, s1, 0x110000
	v_mov_b32_e32 v119, v0
	s_barrier
	s_add_i32 s7, s7, s6
	s_mul_i32 s6, s1, 0x110000
	s_add_u32 s6, s10, s6
	v_ashrrev_i32_e32 v14, 4, v119
	s_mul_i32 s24, s24, 0x88000
	s_mul_hi_u32 s25, s1, 0x88000
	v_ashrrev_i32_e32 v15, 31, v14
	s_addc_u32 s7, s11, s7
	s_add_i32 s25, s25, s24
	s_mul_i32 s1, s1, 0x88000
	v_ashrrev_i32_e32 v16, 3, v119
	v_lshlrev_b32_e32 v58, 4, v119
	v_lshlrev_b64 v[52:53], 8, v[14:15]
	v_add_u32_e32 v20, 32, v14
	s_add_u32 s24, s12, s1
	v_lshlrev_b32_e32 v24, 3, v119
	v_ashrrev_i32_e32 v17, 31, v16
	v_lshl_add_u64 v[6:7], s[6:7], 0, v[52:53]
	v_and_b32_e32 v18, 0xf0, v58
	v_mov_b32_e32 v19, v227
	v_ashrrev_i32_e32 v21, 31, v20
	s_addc_u32 s25, s13, s25
	v_and_b32_e32 v4, 56, v24
	v_lshlrev_b64 v[50:51], 7, v[16:17]
	v_lshl_add_u64 v[56:57], v[6:7], 0, v[18:19]
	v_lshlrev_b64 v[6:7], 8, v[20:21]
	v_lshl_add_u64 v[2:3], s[24:25], 0, v[50:51]
	v_lshlrev_b32_e32 v4, 1, v4
	v_mov_b32_e32 v5, v227
	v_lshl_add_u64 v[6:7], s[6:7], 0, v[6:7]
	v_lshl_add_u64 v[54:55], v[2:3], 0, v[4:5]
	v_lshl_add_u64 v[10:11], v[6:7], 0, v[18:19]
	global_load_dwordx4 v[2:5], v[54:55], off
	global_load_dwordx4 v[6:9], v[56:57], off
	s_nop 0
	global_load_dwordx4 v[10:13], v[10:11], off
	v_ashrrev_i32_e32 v15, 1, v119
	s_movk_i32 s1, 0xffe0
	v_bfe_u32 v136, v119, 5, 1
	v_bfi_b32 v17, s1, v15, v119
	v_mov_b64_e32 v[22:23], s[4:5]
	s_movk_i32 s1, 0x300
	v_mad_i64_i32 v[22:23], s[4:5], v17, s1, v[22:23]
	v_lshlrev_b32_e32 v226, 4, v136
	v_lshl_add_u64 v[22:23], v[22:23], 0, v[226:227]
	global_load_dwordx4 v[86:89], v[22:23], off
	global_load_dwordx4 v[74:77], v[22:23], off offset:32
	global_load_dwordx4 v[70:73], v[22:23], off offset:64
	global_load_dwordx4 v[82:85], v[22:23], off offset:96
	global_load_dwordx4 v[78:81], v[22:23], off offset:128
	global_load_dwordx4 v[66:69], v[22:23], off offset:160
	v_and_b32_e32 v19, 0x1fffff0, v16
	v_lshlrev_b32_e32 v21, 1, v16
	v_and_b32_e32 v17, 0x70, v119
	v_lshrrev_b32_e32 v25, 1, v16
	v_and_b32_e32 v16, 3, v16
	v_lshlrev_b32_e32 v14, 8, v14
	v_and_or_b32 v19, v21, 8, v19
	v_bfe_u32 v24, v24, 5, 1
	v_and_b32_e32 v26, 48, v58
	v_and_or_b32 v16, v25, 4, v16
	v_bitop3_b32 v14, v18, v14, v17 bitop3:0xde
	v_lshlrev_b32_e32 v20, 8, v20
	v_lshrrev_b32_e32 v19, 2, v19
	v_lshl_or_b32 v16, v16, 6, v26
	v_add_u32_e32 v142, 0, v14
	v_bitop3_b32 v14, v18, v20, v17 bitop3:0xde
	v_or_b32_e32 v17, v19, v24
	v_add_u32_e32 v143, 0, v14
	v_lshl_or_b32 v14, v17, 9, v16
	v_and_b32_e32 v137, 31, v119
	v_add_u32_e32 v144, 0, v14
	v_lshlrev_b32_e32 v90, 8, v137
	s_waitcnt vmcnt(0)
	v_and_b32_e32 v132, 63, v119
	s_movk_i32 s1, 0x2000
	s_movk_i32 s6, 0x4000
	s_mov_b32 s4, 0xa000
	s_cmp_lg_u32 0, -1
	s_mul_i32 s24, s31, 0x110000
	s_waitcnt vmcnt(8)
	ds_write_b128 v144, v[2:5]
	s_waitcnt vmcnt(7)
	ds_write_b128 v142, v[6:9] offset:16384
	s_waitcnt vmcnt(6)
	ds_write_b128 v143, v[10:13] offset:16384
	v_and_b32_e32 v10, 0x70, v58
	v_bitop3_b32 v2, v226, v90, v10 bitop3:0xde
	v_add_u32_e32 v145, 0, v2
	s_waitcnt lgkmcnt(0)
	s_barrier
	ds_read_b128 v[2:5], v145 offset:16384
	ds_read_b128 v[6:9], v145 offset:24576
	s_waitcnt vmcnt(5) lgkmcnt(1)
	v_mfma_f32_32x32x16_bf16 v[18:33], v[2:5], v[86:89], 0
	v_or_b32_e32 v2, 32, v226
	v_bitop3_b32 v2, v2, v90, v10 bitop3:0xde
	v_add_u32_e32 v148, 0, v2
	v_lshlrev_b32_e32 v11, 3, v132
	v_lshlrev_b32_e32 v13, 1, v119
	s_mul_hi_i32 s7, s31, 0x110000
	s_mov_b32 s57, s56
	s_waitcnt lgkmcnt(0)
	v_mfma_f32_32x32x16_bf16 v[34:49], v[6:9], v[86:89], 0
	ds_read_b128 v[2:5], v148 offset:16384
	ds_read_b128 v[6:9], v148 offset:24576
	v_and_b32_e32 v130, 0xffffffe0, v15
	s_mov_b32 s58, s56
	s_mov_b32 s59, s56
	s_mov_b32 s60, s56
	s_mov_b32 s61, s56
	s_mov_b32 s62, s56
	s_waitcnt vmcnt(4) lgkmcnt(1)
	v_mfma_f32_32x32x16_bf16 v[18:33], v[2:5], v[74:77], v[18:33]
	v_or_b32_e32 v2, 64, v226
	v_bitop3_b32 v2, v2, v90, v10 bitop3:0xde
	v_add_u32_e32 v147, 0, v2
	s_mov_b32 s63, s56
	s_mov_b32 s64, s56
	s_mov_b32 s65, s56
	s_mov_b32 s66, s56
	s_waitcnt lgkmcnt(0)
	v_mfma_f32_32x32x16_bf16 v[34:49], v[6:9], v[74:77], v[34:49]
	ds_read_b128 v[2:5], v147 offset:16384
	ds_read_b128 v[6:9], v147 offset:24576
	s_mov_b32 s67, s56
	s_mov_b32 s68, s56
	s_mov_b32 s69, s56
	s_mov_b32 s70, s56
	s_mov_b32 s71, s56
	s_mov_b32 s35, 4
	s_waitcnt vmcnt(3) lgkmcnt(1)
	v_mfma_f32_32x32x16_bf16 v[18:33], v[2:5], v[70:73], v[18:33]
	v_and_b32_e32 v2, 0x3fffffc0, v119
	v_lshl_add_u32 v131, v2, 2, 0
	v_or_b32_e32 v2, 0x60, v226
	v_bitop3_b32 v2, v2, v90, v10 bitop3:0xde
	v_add_u32_e32 v146, 0, v2
	ds_read_b128 v[2:5], v146 offset:16384
	v_lshl_add_u32 v138, v137, 2, v131
	s_waitcnt lgkmcnt(1)
	v_mfma_f32_32x32x16_bf16 v[34:49], v[6:9], v[70:73], v[34:49]
	v_and_b32_e32 v6, 0xc0, v58
	v_and_or_b32 v12, v11, 24, v6
	ds_read_b128 v[6:9], v146 offset:24576
	v_mov_b32_e32 v140, 0
	s_waitcnt vmcnt(2) lgkmcnt(1)
	v_mfma_f32_32x32x16_bf16 v[18:33], v[2:5], v[82:85], v[18:33]
	v_or_b32_e32 v2, 0x80, v226
	v_bitop3_b32 v14, v2, v90, v10 bitop3:0xde
	v_add_co_u32_e32 v2, vcc, s1, v54
	s_movk_i32 s1, 0x6000
	s_nop 0
	v_addc_co_u32_e32 v3, vcc, 0, v55, vcc
	global_load_dwordx4 v[58:61], v[2:3], off
	v_add_co_u32_e32 v2, vcc, s6, v56
	v_add_u32_e32 v150, 0, v14
	s_nop 0
	v_addc_co_u32_e32 v3, vcc, 0, v57, vcc
	v_add_co_u32_e32 v4, vcc, s1, v56
	s_waitcnt lgkmcnt(0)
	v_mfma_f32_32x32x16_bf16 v[34:49], v[6:9], v[82:85], v[34:49]
	v_addc_co_u32_e32 v5, vcc, 0, v57, vcc
	global_load_dwordx4 v[62:65], v[2:3], off
	global_load_dwordx4 v[102:105], v[4:5], off
	ds_read_b128 v[2:5], v150 offset:16384
	v_and_b32_e32 v6, 32, v13
	v_and_b32_e32 v7, 0x100, v11
	v_or3_b32 v133, v12, v6, v7
	ds_read_b128 v[6:9], v150 offset:24576
	s_waitcnt vmcnt(4) lgkmcnt(1)
	v_mfma_f32_32x32x16_bf16 v[18:33], v[2:5], v[78:81], v[18:33]
	v_or_b32_e32 v2, 0xa0, v226
	v_bitop3_b32 v2, v2, v90, v10 bitop3:0xde
	v_add_u32_e32 v149, 0, v2
	ds_read_b128 v[2:5], v149 offset:16384
	ds_read_b128 v[90:93], v149 offset:24576
	s_cselect_b32 s1, 0, 0
	v_add_u32_e32 v141, s1, v133
	s_waitcnt lgkmcnt(2)
	v_mfma_f32_32x32x16_bf16 v[34:49], v[6:9], v[78:81], v[34:49]
	s_waitcnt vmcnt(3) lgkmcnt(1)
	v_mfma_f32_32x32x16_bf16 v[18:33], v[2:5], v[66:69], v[18:33]
	v_mov_b64_e32 v[2:3], s[56:57]
	v_mov_b64_e32 v[16:17], s[70:71]
	v_mov_b64_e32 v[4:5], s[58:59]
	v_mov_b64_e32 v[6:7], s[60:61]
	v_mov_b64_e32 v[8:9], s[62:63]
	v_mov_b64_e32 v[10:11], s[64:65]
	v_mov_b64_e32 v[12:13], s[66:67]
	s_waitcnt lgkmcnt(0)
	v_mfma_f32_32x32x16_bf16 v[34:49], v[90:93], v[66:69], v[34:49]
	s_nop 2
	v_max_f32_e32 v90, v19, v19
	v_max_f32_e32 v91, v18, v18
	v_max_f32_e32 v90, v91, v90
	v_max3_f32 v90, v90, v20, v21
	v_max3_f32 v90, v90, v22, v23
	v_max3_f32 v90, v90, v24, v25
	v_max3_f32 v90, v90, v26, v27
	v_max3_f32 v90, v90, v28, v29
	v_max3_f32 v90, v90, v30, v31
	v_max3_f32 v90, v90, v32, v33
	v_max3_f32 v90, v90, v34, v35
	v_max3_f32 v90, v90, v36, v37
	v_max3_f32 v90, v90, v38, v39
	v_max3_f32 v90, v90, v40, v41
	v_max3_f32 v90, v90, v42, v43
	v_max3_f32 v90, v90, v44, v45
	v_max3_f32 v90, v90, v46, v47
	v_max3_f32 v90, v90, v48, v49
	v_mov_b32_e32 v91, v90
	s_nop 1
	v_permlane32_swap_b32_e32 v90, v91
	v_max_f32_e32 v91, v91, v91
	v_max_f32_e32 v90, v90, v90
	v_max_f32_e32 v106, v90, v91
	v_add_f32_e32 v90, 0x7149f2ca, v106
	v_cmp_ge_f32_e32 vcc, s93, v90
	v_add_co_u32_e64 v90, s[4:5], s4, v56
	s_cmp_eq_u64 vcc, exec
	s_nop 0
	v_addc_co_u32_e64 v91, s[4:5], 0, v57, s[4:5]
	v_add_co_u32_e64 v56, s[4:5], s49, v56
	s_cselect_b64 vcc, -1, 0
	s_nop 0
	v_addc_co_u32_e64 v57, s[4:5], 0, v57, s[4:5]
	v_add_co_u32_e64 v54, s[4:5], s6, v54
	global_load_dwordx4 v[94:97], v[90:91], off
	global_load_dwordx4 v[98:101], v[56:57], off
	v_addc_co_u32_e64 v55, s[4:5], 0, v55, s[4:5]
	global_load_dwordx4 v[90:93], v[54:55], off
	v_max_f32_e32 v55, 0xf149f2ca, v106
	v_mov_b32_e32 v54, 0xf149f2ca
	v_cndmask_b32_e32 v118, v55, v54, vcc
	v_mul_f32_e32 v54, 0xbfb8aa3b, v118
	v_fmamk_f32 v18, v18, 0x3fb8aa3b, v54
	v_exp_f32_e32 v128, v18
	v_fmamk_f32 v18, v19, 0x3fb8aa3b, v54
	v_exp_f32_e32 v157, v18
	v_fmamk_f32 v18, v20, 0x3fb8aa3b, v54
	v_exp_f32_e32 v129, v18
	v_fmamk_f32 v18, v21, 0x3fb8aa3b, v54
	v_exp_f32_e32 v158, v18
	v_fmamk_f32 v18, v22, 0x3fb8aa3b, v54
	v_exp_f32_e32 v155, v18
	v_fmamk_f32 v18, v23, 0x3fb8aa3b, v54
	v_exp_f32_e32 v159, v18
	v_fmamk_f32 v18, v24, 0x3fb8aa3b, v54
	v_exp_f32_e32 v156, v18
	v_fmamk_f32 v18, v25, 0x3fb8aa3b, v54
	v_exp_f32_e32 v160, v18
	v_fmamk_f32 v18, v26, 0x3fb8aa3b, v54
	v_exp_f32_e32 v120, v18
	v_fmamk_f32 v18, v27, 0x3fb8aa3b, v54
	v_exp_f32_e32 v124, v18
	v_fmamk_f32 v18, v28, 0x3fb8aa3b, v54
	v_exp_f32_e32 v121, v18
	v_fmamk_f32 v18, v29, 0x3fb8aa3b, v54
	v_exp_f32_e32 v125, v18
	v_fmamk_f32 v18, v30, 0x3fb8aa3b, v54
	s_addk_i32 s1, 0x2000
	s_mul_i32 s6, s0, 0x440000
	v_exp_f32_e32 v122, v18
	v_fmamk_f32 v18, v31, 0x3fb8aa3b, v54
	v_add_u32_e32 v139, s1, v133
	s_mul_hi_i32 s1, s0, 0x440000
	s_add_u32 s6, s6, s24
	v_exp_f32_e32 v126, v18
	v_fmamk_f32 v18, v32, 0x3fb8aa3b, v54
	s_addc_u32 s7, s1, s7
	v_pk_fma_f32 v[106:107], v[40:41], s[92:93], v[54:55] op_sel_hi:[1,0,0]
	v_sub_f32_e32 v40, 0xf149f2ca, v55
	v_exp_f32_e32 v123, v18
	v_lshl_add_u64 v[18:19], s[6:7], 0, v[52:53]
	s_mul_hi_i32 s1, s0, 0x220000
	s_mul_i32 s0, s0, 0x220000
	s_mul_i32 s7, s31, 0x88000
	v_mul_f32_e32 v40, 0x3fb8aa3b, v40
	v_and_b32_e32 v20, 15, v119
	s_mul_hi_i32 s6, s31, 0x88000
	s_add_u32 s0, s0, s7
	s_waitcnt vmcnt(3)
	s_waitcnt vmcnt(5)
	ds_write_b128 v144, v[58:61] offset:8192
	s_waitcnt vmcnt(4)
	ds_write_b128 v142, v[62:65] offset:32768
	s_waitcnt vmcnt(3)
	ds_write_b128 v143, v[102:105] offset:32768
	v_pk_fma_f32 v[102:103], v[48:49], s[92:93], v[54:55] op_sel_hi:[1,0,0]
	v_pk_fma_f32 v[108:109], v[46:47], s[92:93], v[54:55] op_sel_hi:[1,0,0]
	v_pk_fma_f32 v[110:111], v[44:45], s[92:93], v[54:55] op_sel_hi:[1,0,0]
	v_pk_fma_f32 v[104:105], v[42:43], s[92:93], v[54:55] op_sel_hi:[1,0,0]
	v_exp_f32_e32 v40, v40
	v_pk_fma_f32 v[112:113], v[38:39], s[92:93], v[54:55] op_sel_hi:[1,0,0]
	v_pk_fma_f32 v[114:115], v[36:37], s[92:93], v[54:55] op_sel_hi:[1,0,0]
	v_pk_fma_f32 v[116:117], v[34:35], s[92:93], v[54:55] op_sel_hi:[1,0,0]
	v_fmac_f32_e32 v54, 0x3fb8aa3b, v33
	v_lshl_or_b32 v18, v20, 4, v18
	s_addc_u32 s1, s1, s6
	v_exp_f32_e32 v127, v54
	v_cmp_gt_u32_e64 s[4:5], 32, v132
	v_lshl_add_u64 v[132:133], s[18:19], 0, v[18:19]
	v_lshl_add_u64 v[18:19], s[0:1], 0, v[50:51]
	v_and_b32_e32 v20, 7, v119
	v_lshl_or_b32 v18, v20, 4, v18
	v_mov_b64_e32 v[14:15], s[68:69]
	v_lshl_add_u64 v[134:135], s[20:21], 0, v[18:19]
	v_mov_b64_e32 v[32:33], v[16:17]
	v_readlane_b32 s60, v255, 19
	v_readlane_b32 s62, v255, 21
	v_readlane_b32 s64, v255, 23
	v_readlane_b32 s66, v255, 25
	v_cndmask_b32_e64 v151, v40, 1.0, vcc
	v_mov_b64_e32 v[30:31], v[14:15]
	v_mov_b64_e32 v[28:29], v[12:13]
	v_mov_b64_e32 v[26:27], v[10:11]
	v_mov_b64_e32 v[24:25], v[8:9]
	v_mov_b64_e32 v[22:23], v[6:7]
	v_mov_b64_e32 v[20:21], v[4:5]
	v_mov_b64_e32 v[18:19], v[2:3]
	v_readlane_b32 s61, v255, 20
	v_readlane_b32 s63, v255, 22
	v_readlane_b32 s65, v255, 24
	v_readlane_b32 s67, v255, 26
	s_waitcnt lgkmcnt(0)
	s_barrier
	v_add_u32_e32 v144, 0x10000, v144
	v_add_u32_e32 v142, 0x10000, v142
	v_add_u32_e32 v143, 0x10000, v143
.LBB0_582:
	ds_read_b128 v[34:37], v145 offset:32768
	ds_read_b128 v[38:41], v145 offset:40960
	ds_read_b128 v[162:165], v148 offset:32768
	ds_read_b128 v[172:175], v148 offset:40960
	v_exp_f32_e32 v161, v114
	v_add_f32_e32 v114, 0, v128
	s_waitcnt lgkmcnt(3)
	v_mfma_f32_32x32x16_bf16 v[50:65], v[34:37], v[86:89], 0
	v_add_f32_e32 v114, v157, v114
	v_add_f32_e32 v114, v129, v114
	v_add_f32_e32 v114, v158, v114
	v_add_f32_e32 v114, v155, v114
	v_add_f32_e32 v114, v159, v114
	v_add_f32_e32 v114, v156, v114
	v_add_f32_e32 v114, v160, v114
	s_waitcnt lgkmcnt(2)
	v_mfma_f32_32x32x16_bf16 v[34:49], v[38:41], v[86:89], 0
	v_add_f32_e32 v114, v120, v114
	v_add_f32_e32 v114, v124, v114
	v_add_f32_e32 v114, v121, v114
	v_add_f32_e32 v114, v125, v114
	v_exp_f32_e32 v119, v116
	v_add_f32_e32 v114, v122, v114
	v_exp_f32_e32 v154, v117
	s_waitcnt lgkmcnt(1)
	v_mfma_f32_32x32x16_bf16 v[50:65], v[162:165], v[74:77], v[50:65]
	v_add_f32_e32 v114, v126, v114
	v_add_f32_e32 v114, v123, v114
	v_add_f32_e32 v114, v127, v114
	v_exp_f32_e32 v112, v112
	v_add_f32_e32 v114, v119, v114
	v_exp_f32_e32 v113, v113
	v_add_f32_e32 v114, v154, v114
	s_waitcnt lgkmcnt(0)
	v_mfma_f32_32x32x16_bf16 v[34:49], v[172:175], v[74:77], v[34:49]
	ds_read_b128 v[162:165], v147 offset:32768
	ds_read_b128 v[172:175], v147 offset:40960
	v_exp_f32_e32 v106, v106
	v_add_f32_e32 v114, v161, v114
	v_exp_f32_e32 v107, v107
	v_exp_f32_e32 v104, v104
	v_exp_f32_e32 v105, v105
	v_exp_f32_e32 v110, v110
	s_waitcnt lgkmcnt(1)
	v_mfma_f32_32x32x16_bf16 v[50:65], v[162:165], v[70:73], v[50:65]
	v_exp_f32_e32 v111, v111
	v_exp_f32_e32 v108, v108
	v_exp_f32_e32 v109, v109
	v_exp_f32_e32 v102, v102
	v_exp_f32_e32 v103, v103
	s_waitcnt lgkmcnt(0)
	v_mfma_f32_32x32x16_bf16 v[34:49], v[172:175], v[70:73], v[34:49]
	ds_read_b128 v[162:165], v146 offset:32768
	ds_read_b128 v[172:175], v146 offset:40960
	s_waitcnt lgkmcnt(1)
	v_mfma_f32_32x32x16_bf16 v[50:65], v[162:165], v[82:85], v[50:65]
	s_waitcnt lgkmcnt(0)
	v_mfma_f32_32x32x16_bf16 v[34:49], v[172:175], v[82:85], v[34:49]
	ds_read_b128 v[162:165], v150 offset:32768
	ds_read_b128 v[172:175], v150 offset:40960
	s_waitcnt lgkmcnt(1)
	v_mfma_f32_32x32x16_bf16 v[50:65], v[162:165], v[78:81], v[50:65]
	s_waitcnt lgkmcnt(0)
	v_mfma_f32_32x32x16_bf16 v[34:49], v[172:175], v[78:81], v[34:49]
	ds_read_b128 v[162:165], v149 offset:32768
	ds_read_b128 v[172:175], v149 offset:40960
	s_waitcnt lgkmcnt(1)
	v_mfma_f32_32x32x16_bf16 v[50:65], v[162:165], v[66:69], v[50:65]
	v_exp_f32_e32 v162, v115
	s_nop 0
	v_add_f32_e32 v114, v162, v114
	v_add_f32_e32 v114, v112, v114
	v_add_f32_e32 v114, v113, v114
	v_add_f32_e32 v114, v106, v114
	v_add_f32_e32 v114, v107, v114
	v_add_f32_e32 v114, v104, v114
	v_add_f32_e32 v114, v105, v114
	s_waitcnt lgkmcnt(0)
	v_mfma_f32_32x32x16_bf16 v[34:49], v[172:175], v[66:69], v[34:49]
	v_add_f32_e32 v114, v110, v114
	v_add_f32_e32 v114, v111, v114
	v_add_f32_e32 v114, v108, v114
	v_add_f32_e32 v114, v109, v114
	v_add_f32_e32 v114, v102, v114
	v_add_f32_e32 v152, v103, v114
	v_mov_b32_e32 v153, v152
	v_cvt_pk_bf16_f32 v114, v128, v157
	v_cvt_pk_bf16_f32 v115, v129, v158
	v_cvt_pk_bf16_f32 v116, v155, v159
	v_cvt_pk_bf16_f32 v117, v156, v160
	v_cvt_pk_bf16_f32 v120, v120, v124
	v_cvt_pk_bf16_f32 v121, v121, v125
	v_cvt_pk_bf16_f32 v122, v122, v126
	v_cvt_pk_bf16_f32 v123, v123, v127
	v_cvt_pk_bf16_f32 v124, v119, v154
	v_cvt_pk_bf16_f32 v125, v161, v162
	v_cvt_pk_bf16_f32 v126, v112, v113
	v_cvt_pk_bf16_f32 v127, v106, v107
	v_cvt_pk_bf16_f32 v154, v104, v105
	v_cvt_pk_bf16_f32 v155, v110, v111
	v_cvt_pk_bf16_f32 v156, v108, v109
	s_nop 1
	v_permlane32_swap_b32_e32 v152, v153
	v_permlane32_swap_b32_e32 v114, v116
	v_cvt_pk_bf16_f32 v157, v102, v103
	v_permlane32_swap_b32_e32 v154, v156
	v_permlane32_swap_b32_e32 v115, v117
	v_permlane32_swap_b32_e32 v120, v122
	v_permlane32_swap_b32_e32 v121, v123
	v_permlane32_swap_b32_e32 v124, v126
	v_permlane32_swap_b32_e32 v125, v127
	v_permlane32_swap_b32_e32 v155, v157
	s_movk_i32 s0, 0xe000
	v_add_co_u32_e32 v102, vcc, s0, v134
	s_movk_i32 s0, 0xa000
	s_nop 0
	v_addc_co_u32_e32 v103, vcc, -1, v135, vcc
	v_add_co_u32_e32 v106, vcc, s0, v132
	s_movk_i32 s0, 0xc000
	s_nop 0
	v_addc_co_u32_e32 v107, vcc, -1, v133, vcc
	v_add_co_u32_e32 v110, vcc, s0, v132
	global_load_dwordx4 v[102:105], v[102:103], off
	s_nop 0
	v_addc_co_u32_e32 v111, vcc, -1, v133, vcc
	global_load_dwordx4 v[106:109], v[106:107], off
	s_nop 0
	global_load_dwordx4 v[110:113], v[110:111], off
	ds_read_b64_tr_b16 v[158:159], v141 offset:0
	ds_read_b64_tr_b16 v[160:161], v141 offset:0x400
	ds_read_b64_tr_b16 v[162:163], v141 offset:0x800
	ds_read_b64_tr_b16 v[164:165], v141 offset:0xc00
	ds_read_b64_tr_b16 v[172:173], v141 offset:0x1000
	ds_read_b64_tr_b16 v[174:175], v141 offset:0x1400
	ds_read_b64_tr_b16 v[176:177], v141 offset:0x1800
	ds_read_b64_tr_b16 v[178:179], v141 offset:0x1c00
	s_waitcnt lgkmcnt(0)
	s_nop 0
	v_mfma_f32_32x32x16_bf16 v[2:17], v[114:117], v[158:161], v[2:17]
	ds_read_b64_tr_b16 v[158:159], v141 offset:0x200
	ds_read_b64_tr_b16 v[160:161], v141 offset:0x600
	v_mfma_f32_32x32x16_bf16 v[2:17], v[120:123], v[162:165], v[2:17]
	ds_read_b64_tr_b16 v[162:163], v141 offset:0xa00
	ds_read_b64_tr_b16 v[164:165], v141 offset:0xe00
	v_mfma_f32_32x32x16_bf16 v[2:17], v[124:127], v[172:175], v[2:17]
	ds_read_b64_tr_b16 v[172:173], v141 offset:0x1200
	ds_read_b64_tr_b16 v[174:175], v141 offset:0x1600
	v_mfma_f32_32x32x16_bf16 v[2:17], v[154:157], v[176:179], v[2:17]
	ds_read_b64_tr_b16 v[176:177], v141 offset:0x1a00
	ds_read_b64_tr_b16 v[178:179], v141 offset:0x1e00
	s_waitcnt lgkmcnt(0)
	v_mfma_f32_32x32x16_bf16 v[18:33], v[114:117], v[158:161], v[18:33]
	v_max_f32_e32 v114, v51, v51
	v_max_f32_e32 v115, v50, v50
	v_max_f32_e32 v114, v115, v114
	v_max3_f32 v114, v114, v52, v53
	v_max3_f32 v114, v114, v54, v55
	v_max3_f32 v114, v114, v56, v57
	v_max3_f32 v114, v114, v58, v59
	v_max3_f32 v114, v114, v60, v61
	v_max3_f32 v114, v114, v62, v63
	v_mfma_f32_32x32x16_bf16 v[18:33], v[120:123], v[162:165], v[18:33]
	v_max3_f32 v114, v114, v64, v65
	v_max3_f32 v114, v114, v34, v35
	v_max3_f32 v114, v114, v36, v37
	v_max3_f32 v114, v114, v38, v39
	v_max3_f32 v114, v114, v40, v41
	v_max3_f32 v114, v114, v42, v43
	v_max3_f32 v114, v114, v44, v45
	v_max3_f32 v114, v114, v46, v47
	v_mfma_f32_32x32x16_bf16 v[18:33], v[124:127], v[172:175], v[18:33]
	v_max3_f32 v114, v114, v48, v49
	v_mov_b32_e32 v115, v114
	s_nop 1
	v_permlane32_swap_b32_e32 v114, v115
	v_max_f32_e32 v115, v115, v115
	v_max_f32_e32 v114, v114, v114
	v_max_f32_e32 v114, v114, v115
	v_sub_f32_e32 v115, v114, v118
	v_cmp_ge_f32_e32 vcc, s93, v115
	v_max_f32_e32 v115, v118, v118
	v_max_f32_e32 v114, v115, v114
	v_mfma_f32_32x32x16_bf16 v[18:33], v[154:157], v[176:179], v[18:33]
	v_sub_f32_e32 v115, v118, v114
	v_mul_f32_e32 v115, 0x3fb8aa3b, v115
	v_exp_f32_e32 v115, v115
	s_cmp_eq_u64 vcc, exec
	s_cselect_b64 s[6:7], -1, 0
	v_xor_b32_e32 v145, 0x10000, v145
	v_xor_b32_e32 v146, 0x10000, v146
	v_xor_b32_e32 v147, 0x10000, v147
	v_xor_b32_e32 v148, 0x10000, v148
	v_xor_b32_e32 v149, 0x10000, v149
	v_xor_b32_e32 v150, 0x10000, v150
	s_waitcnt vmcnt(3)
	v_cndmask_b32_e64 v154, v115, 1.0, s[6:7]
	v_cmp_gt_f32_e32 vcc, 1.0, v154
	s_waitcnt vmcnt(3)
	ds_write_b128 v144, v[90:93]
	ds_write_b128 v142, v[98:101] offset:16384
	ds_write_b128 v143, v[94:97] offset:16384
	s_cbranch_vccz .LBB0_586
	s_and_saveexec_b64 s[0:1], s[4:5]
	ds_write_b32 v138, v154 offset:49280
	s_or_b64 exec, exec, s[0:1]
	s_waitcnt lgkmcnt(0)
	v_add_u32_e32 v115, v131, v226
	ds_read_b128 v[120:123], v115 offset:49376
	ds_read_b128 v[124:127], v115 offset:49344
	ds_read_b128 v[156:159], v115 offset:49312
	ds_read_b128 v[160:163], v115 offset:49280
	s_waitcnt lgkmcnt(3)
	v_pk_mul_f32 v[14:15], v[14:15], v[120:121]
	s_waitcnt lgkmcnt(2)
	v_pk_mul_f32 v[10:11], v[10:11], v[124:125]
	s_waitcnt lgkmcnt(1)
	v_pk_mul_f32 v[6:7], v[6:7], v[156:157]
	v_pk_mul_f32 v[16:17], v[16:17], v[122:123]
	v_pk_mul_f32 v[12:13], v[12:13], v[126:127]
	v_pk_mul_f32 v[8:9], v[8:9], v[158:159]
	s_waitcnt lgkmcnt(0)
	v_pk_mul_f32 v[4:5], v[4:5], v[162:163]
	v_pk_mul_f32 v[2:3], v[2:3], v[160:161]
	v_pk_mul_f32 v[30:31], v[30:31], v[120:121]
	v_pk_mul_f32 v[26:27], v[26:27], v[124:125]
	v_pk_mul_f32 v[22:23], v[22:23], v[156:157]
	v_pk_mul_f32 v[32:33], v[32:33], v[122:123]
	v_pk_mul_f32 v[28:29], v[28:29], v[126:127]
	v_pk_mul_f32 v[24:25], v[24:25], v[158:159]
	v_pk_mul_f32 v[20:21], v[20:21], v[162:163]
	v_pk_mul_f32 v[18:19], v[18:19], v[160:161]

.LBB0_588:
	ds_read_b64_tr_b16 v[156:157], v139 offset:0
	ds_read_b64_tr_b16 v[158:159], v139 offset:0x400
	ds_read_b64_tr_b16 v[172:173], v139 offset:0x800
	ds_read_b64_tr_b16 v[174:175], v139 offset:0xc00
	ds_read_b64_tr_b16 v[176:177], v139 offset:0x1000
	ds_read_b64_tr_b16 v[178:179], v139 offset:0x1400
	ds_read_b64_tr_b16 v[180:181], v139 offset:0x1800
	ds_read_b64_tr_b16 v[182:183], v139 offset:0x1c00
	s_waitcnt lgkmcnt(0)
	s_nop 0
	v_mfma_f32_32x32x16_bf16 v[2:17], v[114:117], v[156:159], v[2:17]
	ds_read_b64_tr_b16 v[156:157], v139 offset:0x200
	ds_read_b64_tr_b16 v[158:159], v139 offset:0x600
	v_mfma_f32_32x32x16_bf16 v[2:17], v[118:121], v[172:175], v[2:17]
	ds_read_b64_tr_b16 v[172:173], v139 offset:0xa00
	ds_read_b64_tr_b16 v[174:175], v139 offset:0xe00
	v_mfma_f32_32x32x16_bf16 v[2:17], v[122:125], v[176:179], v[2:17]
	ds_read_b64_tr_b16 v[176:177], v139 offset:0x1200
	ds_read_b64_tr_b16 v[178:179], v139 offset:0x1600
	v_mfma_f32_32x32x16_bf16 v[2:17], v[126:129], v[180:183], v[2:17]
	ds_read_b64_tr_b16 v[180:181], v139 offset:0x1a00
	ds_read_b64_tr_b16 v[182:183], v139 offset:0x1e00
	s_waitcnt lgkmcnt(0)
	v_mfma_f32_32x32x16_bf16 v[18:33], v[114:117], v[156:159], v[18:33]
	v_max_f32_e32 v114, v51, v51
	v_max_f32_e32 v115, v50, v50
	v_max_f32_e32 v114, v115, v114
	v_max3_f32 v114, v114, v52, v53
	v_max3_f32 v114, v114, v54, v55
	v_max3_f32 v114, v114, v56, v57
	v_max3_f32 v114, v114, v58, v59
	v_max3_f32 v114, v114, v60, v61
	v_max3_f32 v114, v114, v62, v63
	v_mfma_f32_32x32x16_bf16 v[18:33], v[118:121], v[172:175], v[18:33]
	v_max3_f32 v114, v114, v64, v65
	v_max3_f32 v114, v114, v34, v35
	v_max3_f32 v114, v114, v36, v37
	v_max3_f32 v114, v114, v38, v39
	v_max3_f32 v114, v114, v40, v41
	v_max3_f32 v114, v114, v42, v43
	v_max3_f32 v114, v114, v44, v45
	v_max3_f32 v114, v114, v46, v47
	v_mfma_f32_32x32x16_bf16 v[18:33], v[122:125], v[176:179], v[18:33]
	v_max3_f32 v114, v114, v48, v49
	v_mov_b32_e32 v115, v114
	s_nop 1
	v_permlane32_swap_b32_e32 v114, v115
	v_max_f32_e32 v115, v115, v115
	v_max_f32_e32 v114, v114, v114
	v_max_f32_e32 v114, v114, v115
	v_sub_f32_e32 v115, v114, v155
	v_cmp_ge_f32_e32 vcc, s93, v115
	v_max_f32_e32 v115, v155, v155
	v_max_f32_e32 v114, v115, v114
	v_mfma_f32_32x32x16_bf16 v[18:33], v[126:129], v[180:183], v[18:33]
	v_sub_f32_e32 v115, v155, v114
	v_mul_f32_e32 v115, 0x3fb8aa3b, v115
	v_exp_f32_e32 v115, v115
	s_cmp_eq_u64 vcc, exec
	s_cselect_b64 s[6:7], -1, 0
	s_waitcnt vmcnt(3)
	v_cndmask_b32_e64 v119, v115, 1.0, s[6:7]
	v_cmp_gt_f32_e32 vcc, 1.0, v119
	s_waitcnt vmcnt(2)
	ds_write_b128 v144, v[102:105] offset:8192
	s_waitcnt vmcnt(1)
	ds_write_b128 v142, v[106:109] offset:32768
	s_waitcnt vmcnt(0)
	ds_write_b128 v143, v[110:113] offset:32768
	s_cbranch_vccz .LBB0_592
	s_and_saveexec_b64 s[24:25], s[4:5]
	ds_write_b32 v138, v119 offset:49280
	s_or_b64 exec, exec, s[24:25]
	s_waitcnt lgkmcnt(0)
	v_add_u32_e32 v115, v131, v226
	ds_read_b128 v[102:105], v115 offset:49376
	ds_read_b128 v[106:109], v115 offset:49344
	ds_read_b128 v[110:113], v115 offset:49312
	ds_read_b128 v[120:123], v115 offset:49280
	s_waitcnt lgkmcnt(3)
	v_pk_mul_f32 v[14:15], v[14:15], v[102:103]
	s_waitcnt lgkmcnt(2)
	v_pk_mul_f32 v[10:11], v[10:11], v[106:107]
	s_waitcnt lgkmcnt(1)
	v_pk_mul_f32 v[6:7], v[6:7], v[110:111]
	v_pk_mul_f32 v[16:17], v[16:17], v[104:105]
	v_pk_mul_f32 v[12:13], v[12:13], v[108:109]
	v_pk_mul_f32 v[8:9], v[8:9], v[112:113]
	s_waitcnt lgkmcnt(0)
	v_pk_mul_f32 v[4:5], v[4:5], v[122:123]
	v_pk_mul_f32 v[2:3], v[2:3], v[120:121]
	v_pk_mul_f32 v[30:31], v[30:31], v[102:103]
	v_pk_mul_f32 v[26:27], v[26:27], v[106:107]
	v_pk_mul_f32 v[22:23], v[22:23], v[110:111]
	v_pk_mul_f32 v[32:33], v[32:33], v[104:105]
	v_pk_mul_f32 v[28:29], v[28:29], v[108:109]
	v_pk_mul_f32 v[24:25], v[24:25], v[112:113]
	v_pk_mul_f32 v[20:21], v[20:21], v[122:123]
	v_pk_mul_f32 v[18:19], v[18:19], v[120:121]
.LBB0_592:
	v_cndmask_b32_e64 v118, v114, v155, s[6:7]
	v_mul_f32_e32 v102, 0xbfb8aa3b, v118
	v_mov_b32_e32 v103, v102
	v_fmamk_f32 v50, v50, 0x3fb8aa3b, v102
	v_fmamk_f32 v51, v51, 0x3fb8aa3b, v102
	v_fmamk_f32 v52, v52, 0x3fb8aa3b, v102
	v_fmamk_f32 v53, v53, 0x3fb8aa3b, v102
	v_fmamk_f32 v54, v54, 0x3fb8aa3b, v102
	v_fmamk_f32 v55, v55, 0x3fb8aa3b, v102
	v_fmamk_f32 v56, v56, 0x3fb8aa3b, v102
	v_fmamk_f32 v57, v57, 0x3fb8aa3b, v102
	v_fmamk_f32 v58, v58, 0x3fb8aa3b, v102
	v_fmamk_f32 v59, v59, 0x3fb8aa3b, v102
	v_fmamk_f32 v60, v60, 0x3fb8aa3b, v102
	v_fmamk_f32 v61, v61, 0x3fb8aa3b, v102
	v_fmamk_f32 v62, v62, 0x3fb8aa3b, v102
	v_fmamk_f32 v63, v63, 0x3fb8aa3b, v102
	v_fmamk_f32 v64, v64, 0x3fb8aa3b, v102
	v_fmac_f32_e32 v103, 0x3fb8aa3b, v65
	v_exp_f32_e32 v128, v50
	v_exp_f32_e32 v157, v51
	v_exp_f32_e32 v129, v52
	v_exp_f32_e32 v158, v53
	v_exp_f32_e32 v155, v54
	v_exp_f32_e32 v159, v55
	v_exp_f32_e32 v156, v56
	v_exp_f32_e32 v160, v57
	v_exp_f32_e32 v120, v58
	v_exp_f32_e32 v124, v59
	v_exp_f32_e32 v121, v60
	v_exp_f32_e32 v125, v61
	v_exp_f32_e32 v122, v62
	v_exp_f32_e32 v126, v63
	v_exp_f32_e32 v123, v64
	v_exp_f32_e32 v127, v103
	v_pk_fma_f32 v[116:117], v[34:35], s[92:93], v[102:103] op_sel_hi:[1,0,0]
	v_add_f32_e32 v34, v152, v153
	v_fmac_f32_e32 v34, v151, v140
	v_add_f32_e32 v140, v161, v162
	v_pk_fma_f32 v[114:115], v[36:37], s[92:93], v[102:103] op_sel_hi:[1,0,0]
	v_pk_fma_f32 v[112:113], v[38:39], s[92:93], v[102:103] op_sel_hi:[1,0,0]
	v_pk_fma_f32 v[106:107], v[40:41], s[92:93], v[102:103] op_sel_hi:[1,0,0]
	v_pk_fma_f32 v[104:105], v[42:43], s[92:93], v[102:103] op_sel_hi:[1,0,0]
	v_pk_fma_f32 v[110:111], v[44:45], s[92:93], v[102:103] op_sel_hi:[1,0,0]
	v_pk_fma_f32 v[108:109], v[46:47], s[92:93], v[102:103] op_sel_hi:[1,0,0]
	v_pk_fma_f32 v[102:103], v[48:49], s[92:93], v[102:103] op_sel_hi:[1,0,0]
	v_fmac_f32_e32 v140, v34, v154
	v_lshl_add_u64 v[132:133], v[132:133], 0, s[76:77]
	v_lshl_add_u64 v[134:135], v[134:135], 0, s[90:91]
	v_xor_b32_e32 v141, 0x10000, v141
	v_xor_b32_e32 v139, 0x10000, v139
	v_xor_b32_e32 v144, 0x10000, v144
	v_xor_b32_e32 v142, 0x10000, v142
	v_xor_b32_e32 v143, 0x10000, v143
	s_add_i32 s35, s35, 2
	s_and_b64 vcc, exec, s[0:1]
	s_waitcnt lgkmcnt(0)
	s_barrier
	s_cbranch_vccnz .LBB0_594
	v_mov_b32_e32 v151, v119
	s_branch .LBB0_582
